# v030 plus tile-loop top: first K-fragment ds_reads issued before the next tile's global K/V loads and their address arithmetic
# baseline (speedup 1.0000x reference)
; #define LAS __attribute__((address_space(3)))
; #define SBAR() __builtin_amdgcn_sched_barrier(0)
; #define SLOAD_A(k0) do { const bf16_t* vp_ = Vh + (long)(k0) * LDK + toff; const bf16_t* kp_ = Kh + (long)(k0) * LDK + toff; \
;     sa0 = *(const bf16x8*)kp_; sa1 = *(const bf16x8*)(kp_ + 32L * LDK); sa2 = *(const bf16x8*)vp_; sa3 = *(const bf16x8*)(vp_ + 128); } while (0)
; __device__ __forceinline__ void qkt(f32x16& p0, f32x16& p1, const LAS char* Ks, const bf16x8* qr, int r32, int hi) {
;   p0 = f32x16{}; p1 = f32x16{};
; #pragma unroll
;   for (int d0 = 0; d0 < 8; ++d0) { int cb = (d0 * 16 + hi * 8) * 2;
;     bf16x8 b0 = *(const LAS bf16x8*)(Ks + KSWZ(r32, cb));
;     bf16x8 b1 = *(const LAS bf16x8*)(Ks + KSWZ(32 + r32, cb));
;     p0 = __builtin_amdgcn_mfma_f32_32x32x16_bf16(b0, qr[d0], p0, 0, 0, 0);
;     p1 = __builtin_amdgcn_mfma_f32_32x32x16_bf16(b1, qr[d0], p1, 0, 0, 0); }
; }
; template <int LDQ, int LDK, int LDO>
; __device__ __forceinline__ void attn_body256(const bf16_t* __restrict__ Qb, const bf16_t* __restrict__ Kh, const bf16_t* __restrict__ Vh, float* __restrict__ Ob, int seq, LAS char* lds) {
;     ...
;     if (j + 1 < NT) SLOAD_A((j + 1) * KVBLK);
;     SBAR(); qkt(p0, p1, K_lds + (j & 1) * SHM_K2, qr, r32, hi);
.LBB0_934:
	s_add_i32 s87, s10, 1
	s_and_b32 s88, s10, 1
	v_lshl_add_u32 v2, s88, 14, v239
	v_add_u32_e32 v136, v2, v215
	ds_read_b128 v[132:135], v136
	ds_read_b128 v[136:139], v136 offset:8192
	v_add_u32_e32 v222, v2, v233
	ds_read_b128 v[250:253], v222
	ds_read_b128 v[222:225], v222 offset:8192
	v_add_u32_e32 v246, v2, v234
	s_cmp_lg_u32 s82, 0x177e000
	s_cselect_b64 s[84:85], -1, 0
	s_cmp_eq_u32 s82, 0x177e000
	v_lshl_add_u64 v[220:221], v[216:217], 0, s[82:83]
	s_cbranch_scc1 .LBB0_936
	v_lshl_add_u64 v[140:141], v[218:219], 0, s[82:83]
	v_add_co_u32_e32 v142, vcc, 0xc3000, v140
	s_nop 1
	v_addc_co_u32_e32 v143, vcc, 0, v141, vcc
	v_add_co_u32_e32 v140, vcc, 0x124000, v140
	s_nop 1
	v_addc_co_u32_e32 v141, vcc, 0, v141, vcc
	global_load_dwordx4 v[204:207], v[142:143], off
	global_load_dwordx4 v[208:211], v[140:141], off
	v_add_co_u32_e32 v140, vcc, 0xc4000, v220
	s_nop 1
	v_addc_co_u32_e32 v141, vcc, 0, v221, vcc
	global_load_dwordx4 v[196:199], v[140:141], off
	global_load_dwordx4 v[200:203], v[140:141], off offset:256
.LBB0_936:
	s_waitcnt lgkmcnt(3)
	v_mfma_f32_32x32x16_bf16 v[148:163], v[132:135], v[164:167], 0
	s_mov_b32 s8, 0x42b504f3
	s_waitcnt lgkmcnt(2)
	v_mfma_f32_32x32x16_bf16 v[132:147], v[136:139], v[164:167], 0
	s_waitcnt lgkmcnt(1)
	v_mfma_f32_32x32x16_bf16 v[148:163], v[250:253], v[168:171], v[148:163]
	ds_read_b128 v[250:253], v246 offset:8192
	s_waitcnt lgkmcnt(1)
	v_mfma_f32_32x32x16_bf16 v[132:147], v[222:225], v[168:171], v[132:147]
	ds_read_b128 v[222:225], v246
	v_add_u32_e32 v246, v2, v235
	s_waitcnt lgkmcnt(1)
	v_mfma_f32_32x32x16_bf16 v[132:147], v[250:253], v[172:175], v[132:147]
	ds_read_b128 v[250:253], v246 offset:8192
	s_waitcnt lgkmcnt(1)
	v_mfma_f32_32x32x16_bf16 v[148:163], v[222:225], v[172:175], v[148:163]
	ds_read_b128 v[222:225], v246
	v_add_u32_e32 v246, v2, v236
	s_waitcnt lgkmcnt(1)
	v_mfma_f32_32x32x16_bf16 v[132:147], v[250:253], v[176:179], v[132:147]
	ds_read_b128 v[250:253], v246 offset:8192
	s_waitcnt lgkmcnt(1)
	v_mfma_f32_32x32x16_bf16 v[148:163], v[222:225], v[176:179], v[148:163]
	ds_read_b128 v[222:225], v246
	v_add_u32_e32 v246, v2, v237
	s_waitcnt lgkmcnt(1)
	v_mfma_f32_32x32x16_bf16 v[132:147], v[250:253], v[180:183], v[132:147]
	ds_read_b128 v[250:253], v246 offset:8192
	s_waitcnt lgkmcnt(1)
	v_mfma_f32_32x32x16_bf16 v[148:163], v[222:225], v[180:183], v[148:163]
	ds_read_b128 v[222:225], v246
	v_add_u32_e32 v246, v2, v238
	v_add_u32_e32 v2, v2, v242
	s_waitcnt lgkmcnt(1)
	v_mfma_f32_32x32x16_bf16 v[132:147], v[250:253], v[184:187], v[132:147]
	ds_read_b128 v[250:253], v246 offset:8192
	s_waitcnt lgkmcnt(1)
	v_mfma_f32_32x32x16_bf16 v[148:163], v[222:225], v[184:187], v[148:163]
	ds_read_b128 v[222:225], v246
	s_waitcnt lgkmcnt(1)
	v_mfma_f32_32x32x16_bf16 v[132:147], v[250:253], v[188:191], v[132:147]
	ds_read_b128 v[250:253], v2 offset:8192
	s_waitcnt lgkmcnt(1)
	v_mfma_f32_32x32x16_bf16 v[148:163], v[222:225], v[188:191], v[148:163]
	ds_read_b128 v[222:225], v2
	s_waitcnt lgkmcnt(0)
; #define SBAR() __builtin_amdgcn_sched_barrier(0)
; #define SLOAD_A(k0) do { const bf16_t* vp_ = Vh + (long)(k0) * LDK + toff; const bf16_t* kp_ = Kh + (long)(k0) * LDK + toff; \
;     sa0 = *(const bf16x8*)kp_; sa1 = *(const bf16x8*)(kp_ + 32L * LDK); sa2 = *(const bf16x8*)vp_; sa3 = *(const bf16x8*)(vp_ + 128); } while (0)
; __device__ __forceinline__ void partialSM(f32x16& p0, f32x16& p1, float& m_reg, float& mn, float& alpha) {
;   constexpr float C = SCALE * 1.4426950408889634f;
;   float pmax = p0[0]; for (int r = 1; r < 16; ++r) pmax = fmaxf(pmax, p0[r]); for (int r = 0; r < 16; ++r) pmax = fmaxf(pmax, p1[r]);
;   { auto rr = __builtin_amdgcn_permlane32_swap(__float_as_uint(pmax), __float_as_uint(pmax), false, false);
;     pmax = fmaxf(__uint_as_float(rr[0]), __uint_as_float(rr[1])); }
;   if (__builtin_expect(__all(pmax - m_reg <= THR / SCALE), 1)) { mn = m_reg; alpha = 1.f; }
;   else { mn = fmaxf(m_reg, pmax); alpha = __builtin_amdgcn_exp2f((m_reg - mn) * C); m_reg = mn; }
;   float mnC = -mn * C;
;   for (int r = 0; r < 16; ++r) p0[r] = fmaf(p0[r], C, mnC); for (int r = 0; r < 16; ++r) p1[r] = fmaf(p1[r], C, mnC);
;   for (int r = 0; r < 16; ++r) p0[r] = __builtin_amdgcn_exp2f(p0[r]);
; }
; __device__ __forceinline__ void finishSM(f32x16& p0, f32x16& p1, float alpha, float& l_reg, bf16x8& pa0, bf16x8& pa1, bf16x8& pa2, bf16x8& pa3) {
;   for (int r = 0; r < 16; ++r) p1[r] = __builtin_amdgcn_exp2f(p1[r]);
;   float ps = 0; for (int r = 0; r < 16; ++r) ps += p0[r]; for (int r = 0; r < 16; ++r) ps += p1[r];
;   { auto rr = __builtin_amdgcn_permlane32_swap(__float_as_uint(ps), __float_as_uint(ps), false, false);
;     ps = __uint_as_float(rr[0]) + __uint_as_float(rr[1]); }
;   l_reg = l_reg * alpha + ps;
;     ...
;   PK4(p0, 0, pa0); PK4(p0, 8, pa1); PK4(p1, 0, pa2); PK4(p1, 8, pa3);
;     ...
; }
; template <int LDQ, int LDK, int LDO>
; __device__ __forceinline__ void attn_body256(const bf16_t* __restrict__ Qb, const bf16_t* __restrict__ Kh, const bf16_t* __restrict__ Vh, float* __restrict__ Ob, int seq, LAS char* lds) {
;     ...
;     if (j + 1 < NT) SLOAD_A((j + 1) * KVBLK);
;     SBAR(); qkt(p0, p1, K_lds + (j & 1) * SHM_K2, qr, r32, hi);
;     partialSM(p0, p1, m_reg, mn, al);
;     finishSM(p0, p1, al, l_reg, pa0, pa1, pa2, pa3); SBAR();
;     if (j + 1 < NT) { asm volatile("s_waitcnt vmcnt(0)" ::: "memory"); SWRITE_A((j + 1) & 1); SLOAD_B((j + 1) * KVBLK); }
	v_mfma_f32_32x32x16_bf16 v[148:163], v[222:225], v[192:195], v[148:163]
	v_mfma_f32_32x32x16_bf16 v[132:147], v[250:253], v[192:195], v[132:147]
	s_nop 9
	v_max_f32_e32 v2, v149, v149
	v_max_f32_e32 v222, v148, v148
	v_max_f32_e32 v2, v222, v2
	v_max3_f32 v2, v2, v150, v151
	v_max3_f32 v2, v2, v152, v153
	v_max3_f32 v2, v2, v154, v155
	v_max3_f32 v2, v2, v156, v157
	v_max3_f32 v2, v2, v158, v159
	v_max3_f32 v2, v2, v160, v161
	v_max3_f32 v2, v2, v162, v163
	v_max3_f32 v2, v2, v132, v133
	v_max3_f32 v2, v2, v134, v135
	v_max3_f32 v2, v2, v136, v137
	v_max3_f32 v2, v2, v138, v139
	v_max3_f32 v2, v2, v140, v141
	v_max3_f32 v2, v2, v142, v143
	v_max3_f32 v2, v2, v144, v145
	v_max3_f32 v2, v2, v146, v147
	v_mov_b32_e32 v222, v2
	s_nop 1
	v_permlane32_swap_b32_e32 v2, v222
	v_max_f32_e32 v222, v222, v222
	v_max_f32_e32 v2, v2, v2
	v_max_f32_e32 v2, v2, v222
	v_sub_f32_e32 v222, v2, v248
	v_cmp_ge_f32_e32 vcc, s8, v222
	s_cmp_eq_u64 vcc, exec
	v_max_f32_e32 v222, v248, v248
	s_cselect_b64 s[10:11], -1, 0
	v_max_f32_e32 v249, v222, v2
	v_cndmask_b32_e64 v2, v249, v248, s[10:11]
	v_mul_f32_e32 v222, 0xbe0293ee, v2
	v_fmamk_f32 v148, v148, 0x3e0293ee, v222
	v_fmamk_f32 v149, v149, 0x3e0293ee, v222
	v_fmamk_f32 v150, v150, 0x3e0293ee, v222
	v_fmamk_f32 v151, v151, 0x3e0293ee, v222
	v_fmamk_f32 v152, v152, 0x3e0293ee, v222
	v_fmamk_f32 v153, v153, 0x3e0293ee, v222
	v_fmamk_f32 v154, v154, 0x3e0293ee, v222
	v_fmamk_f32 v155, v155, 0x3e0293ee, v222
	v_fmamk_f32 v156, v156, 0x3e0293ee, v222
	v_fmamk_f32 v157, v157, 0x3e0293ee, v222
	v_fmamk_f32 v158, v158, 0x3e0293ee, v222
	v_fmamk_f32 v159, v159, 0x3e0293ee, v222
	v_fmamk_f32 v160, v160, 0x3e0293ee, v222
	v_fmamk_f32 v161, v161, 0x3e0293ee, v222
	v_fmamk_f32 v162, v162, 0x3e0293ee, v222
	v_fmamk_f32 v163, v163, 0x3e0293ee, v222
	v_fmamk_f32 v132, v132, 0x3e0293ee, v222
	v_fmamk_f32 v133, v133, 0x3e0293ee, v222
	v_fmamk_f32 v134, v134, 0x3e0293ee, v222
	v_fmamk_f32 v135, v135, 0x3e0293ee, v222
	v_fmamk_f32 v136, v136, 0x3e0293ee, v222
	v_fmamk_f32 v137, v137, 0x3e0293ee, v222
	v_fmamk_f32 v138, v138, 0x3e0293ee, v222
	v_fmamk_f32 v139, v139, 0x3e0293ee, v222
	v_fmamk_f32 v140, v140, 0x3e0293ee, v222
	v_fmamk_f32 v141, v141, 0x3e0293ee, v222
	v_fmamk_f32 v142, v142, 0x3e0293ee, v222
	v_fmamk_f32 v143, v143, 0x3e0293ee, v222
	v_fmamk_f32 v144, v144, 0x3e0293ee, v222
	v_fmamk_f32 v145, v145, 0x3e0293ee, v222
	v_fmamk_f32 v146, v146, 0x3e0293ee, v222
	v_fmac_f32_e32 v222, 0x3e0293ee, v147
	v_exp_f32_e32 v147, v148
	v_exp_f32_e32 v148, v149
	v_exp_f32_e32 v149, v150
	v_exp_f32_e32 v150, v151
	v_exp_f32_e32 v151, v152
	v_exp_f32_e32 v152, v153
	v_exp_f32_e32 v153, v154
	v_exp_f32_e32 v154, v155
	v_exp_f32_e32 v155, v156
	v_exp_f32_e32 v156, v157
	v_exp_f32_e32 v157, v158
	v_exp_f32_e32 v158, v159
	v_exp_f32_e32 v159, v160
	v_exp_f32_e32 v160, v161
	v_exp_f32_e32 v161, v162
	v_exp_f32_e32 v162, v163
	v_exp_f32_e32 v163, v132
	v_add_f32_e32 v132, 0, v147
	v_add_f32_e32 v132, v148, v132
	v_add_f32_e32 v132, v149, v132
	v_add_f32_e32 v132, v150, v132
	v_add_f32_e32 v132, v151, v132
	v_add_f32_e32 v132, v152, v132
	v_add_f32_e32 v132, v153, v132
	v_add_f32_e32 v132, v154, v132
	v_add_f32_e32 v132, v155, v132
	v_add_f32_e32 v132, v156, v132
	v_add_f32_e32 v132, v157, v132
	v_add_f32_e32 v132, v158, v132
	v_add_f32_e32 v132, v159, v132
	v_exp_f32_e32 v223, v133
	v_add_f32_e32 v132, v160, v132
	v_exp_f32_e32 v224, v134
	v_add_f32_e32 v132, v161, v132
	v_exp_f32_e32 v225, v135
	v_add_f32_e32 v132, v162, v132
	v_exp_f32_e32 v250, v136
	v_add_f32_e32 v132, v163, v132
	v_exp_f32_e32 v251, v137
	v_add_f32_e32 v132, v223, v132
	v_exp_f32_e32 v252, v138
	v_add_f32_e32 v132, v224, v132
	v_exp_f32_e32 v253, v139
	v_add_f32_e32 v132, v225, v132
	v_exp_f32_e32 v254, v140
	v_add_f32_e32 v132, v250, v132
	v_exp_f32_e32 v0, v141
	v_add_f32_e32 v132, v251, v132
	v_exp_f32_e32 v1, v142
	v_add_f32_e32 v132, v252, v132
	v_exp_f32_e32 v227, v143
	v_add_f32_e32 v132, v253, v132
	v_exp_f32_e32 v228, v144
	v_add_f32_e32 v132, v254, v132
	v_exp_f32_e32 v229, v145
	v_add_f32_e32 v132, v0, v132
	v_exp_f32_e32 v230, v146
	v_add_f32_e32 v132, v1, v132
	v_exp_f32_e32 v222, v222
	v_add_f32_e32 v132, v227, v132
	v_add_f32_e32 v132, v228, v132
	v_add_f32_e32 v132, v229, v132
	v_add_f32_e32 v132, v230, v132
	v_add_f32_e32 v246, v222, v132
	v_mov_b32_e32 v247, v246
	v_cvt_pk_bf16_f32 v132, v147, v148
	v_cvt_pk_bf16_f32 v133, v149, v150
	v_cvt_pk_bf16_f32 v134, v151, v152
	v_cvt_pk_bf16_f32 v135, v153, v154
	v_cvt_pk_bf16_f32 v136, v155, v156
	v_cvt_pk_bf16_f32 v137, v157, v158
	v_cvt_pk_bf16_f32 v138, v159, v160
	v_cvt_pk_bf16_f32 v139, v161, v162
	v_cvt_pk_bf16_f32 v140, v163, v223
	v_cvt_pk_bf16_f32 v141, v224, v225
	v_cvt_pk_bf16_f32 v142, v250, v251
	v_cvt_pk_bf16_f32 v143, v252, v253
	v_cvt_pk_bf16_f32 v144, v254, v0
	v_cvt_pk_bf16_f32 v145, v1, v227
	v_cvt_pk_bf16_f32 v146, v228, v229
	v_cvt_pk_bf16_f32 v147, v230, v222
	s_nop 1
	v_permlane32_swap_b32_e32 v246, v247
	v_permlane32_swap_b32_e32 v132, v134
	v_permlane32_swap_b32_e32 v133, v135
	v_permlane32_swap_b32_e32 v136, v138
	v_permlane32_swap_b32_e32 v137, v139
	v_permlane32_swap_b32_e32 v140, v142
	v_permlane32_swap_b32_e32 v141, v143
	v_permlane32_swap_b32_e32 v144, v146
	v_permlane32_swap_b32_e32 v145, v147
	v_cndmask_b32_e64 v0, 0, 1, s[84:85]
	v_cmp_ne_u32_e64 s[8:9], 1, v0
	s_andn2_b64 vcc, exec, s[84:85]
	s_cbranch_vccnz .LBB0_938
	s_and_b32 s84, s87, 1
	v_lshl_add_u32 v1, s84, 14, v240
	v_add_co_u32_e32 v148, vcc, 0x125000, v220
	s_waitcnt vmcnt(0)
	v_lshl_add_u32 v0, s84, 15, v241
	s_waitcnt vmcnt(1)
	ds_write_b128 v1, v[204:207]
	s_waitcnt vmcnt(0)
	ds_write_b128 v1, v[208:211] offset:8192
	s_waitcnt vmcnt(1)
	ds_write_b128 v0, v[196:199]
	s_waitcnt vmcnt(0)
	ds_write_b128 v0, v[200:203] offset:2048
	v_addc_co_u32_e32 v149, vcc, 0, v221, vcc
	global_load_dwordx4 v[204:207], v[148:149], off
	global_load_dwordx4 v[208:211], v[148:149], off offset:256
